# router row pass: modulation-vector waits moved to their (rare) reload path so the next tile's row prefetch is not waited for mid-tile
# speedup vs baseline: 1.0142x; 1.0122x over previous
.LBB0_1543:
	s_ashr_i32 s12, s26, 12
	s_mulk_i32 s12, 0x1100
	s_and_b32 s13, s26, 0xffe
	s_add_i32 s14, s12, s13
	s_and_b64 s[12:13], s[4:5], exec
	s_cselect_b32 s16, s26, s14
	s_mul_hi_i32 s12, s16, 0x78787879
	s_lshr_b32 s13, s12, 31
	s_ashr_i32 s12, s12, 11
	s_add_i32 s12, s12, s13
	s_mul_i32 s13, s12, 0xffffef00
	s_add_i32 s13, s13, s16
	s_cmpk_lt_i32 s13, 0x1000
	s_cselect_b32 s12, s12, 8
	s_cmp_eq_u32 s12, s28
	s_cbranch_scc1 .LBB0_1545
	s_mov_b32 s14, 35
	s_ashr_i32 s15, s14, 31
	s_lshl_b64 s[14:15], s[14:15], 3
	s_add_u32 s14, s0, s14
	s_addc_u32 s15, s1, s15
	s_load_dwordx2 s[14:15], s[14:15], 0x0
	s_mul_i32 s13, s73, 9
	s_add_i32 s13, s12, s13
	s_mul_i32 s18, s13, 0x1800
	s_ashr_i32 s19, s18, 31
	s_lshl_b64 s[18:19], s[18:19], 2
	s_waitcnt lgkmcnt(0)
	s_add_u32 s14, s14, s18
	s_addc_u32 s15, s15, s19
	v_lshl_add_u64 v[74:75], s[14:15], 0, v[0:1]
	s_mov_b32 s13, 0x504000
	v_add_co_u32_e32 v76, vcc, s13, v74
	s_mov_b64 s[14:15], 0x504000
	s_nop 0
	v_addc_co_u32_e32 v77, vcc, 0, v75, vcc
	global_load_dwordx4 v[90:93], v[76:77], off
	v_lshl_add_u64 v[76:77], v[74:75], 0, s[14:15]
	s_mov_b64 s[14:15], 0x503000
	s_mov_b32 s13, 0x503000
	v_lshl_add_u64 v[78:79], v[74:75], 0, s[14:15]
	v_add_co_u32_e32 v74, vcc, s13, v74
	global_load_dwordx4 v[94:97], v[76:77], off offset:16
	global_load_dwordx4 v[98:101], v[76:77], off offset:32
	global_load_dwordx4 v[102:105], v[144:145], off offset:48
	global_load_dwordx4 v[106:109], v[144:145], off offset:32
	global_load_dwordx4 v[110:113], v[76:77], off offset:48
	global_load_dwordx4 v[114:117], v[144:145], off offset:16
	global_load_dwordx4 v[118:121], v[144:145], off
	v_addc_co_u32_e32 v75, vcc, 0, v75, vcc
	global_load_dwordx4 v[74:77], v[74:75], off
	s_nop 0
	global_load_dwordx4 v[86:89], v[78:79], off offset:48
	global_load_dwordx4 v[82:85], v[78:79], off offset:32
	s_nop 0
	global_load_dwordx4 v[78:81], v[78:79], off offset:16
	s_mov_b32 s28, s12
	s_waitcnt vmcnt(11)
	v_pk_add_f32 v[92:93], v[92:93], 1.0 op_sel_hi:[1,0]
	v_pk_add_f32 v[90:91], v[90:91], 1.0 op_sel_hi:[1,0]
	s_waitcnt vmcnt(10)
	v_pk_add_f32 v[96:97], v[96:97], 1.0 op_sel_hi:[1,0]
	v_pk_add_f32 v[94:95], v[94:95], 1.0 op_sel_hi:[1,0]
	s_waitcnt vmcnt(9)
	v_pk_add_f32 v[100:101], v[100:101], 1.0 op_sel_hi:[1,0]
	v_pk_add_f32 v[98:99], v[98:99], 1.0 op_sel_hi:[1,0]
	s_waitcnt vmcnt(6)
	v_pk_add_f32 v[112:113], v[112:113], 1.0 op_sel_hi:[1,0]
	v_pk_add_f32 v[110:111], v[110:111], 1.0 op_sel_hi:[1,0]
	s_waitcnt vmcnt(4)
	v_pk_mul_f32 v[92:93], v[120:121], v[92:93]
	v_pk_mul_f32 v[90:91], v[118:119], v[90:91]
	v_pk_mul_f32 v[96:97], v[116:117], v[96:97]
	v_pk_mul_f32 v[94:95], v[114:115], v[94:95]
	v_pk_mul_f32 v[100:101], v[108:109], v[100:101]
	v_pk_mul_f32 v[98:99], v[106:107], v[98:99]
	v_pk_mul_f32 v[104:105], v[104:105], v[112:113]
	v_pk_mul_f32 v[102:103], v[102:103], v[110:111]
	s_waitcnt vmcnt(0)

.LBB0_1547:
	v_lshlrev_b32_e32 v157, 16, v137
	v_lshlrev_b32_e32 v156, 16, v136
	v_and_b32_e32 v137, 0xffff0000, v137
	v_and_b32_e32 v136, 0xffff0000, v136
	v_pk_mul_f32 v[172:173], v[136:137], v[136:137]
	v_lshlrev_b32_e32 v154, 16, v134
	v_pk_fma_f32 v[172:173], v[156:157], v[156:157], v[172:173]
	v_and_b32_e32 v155, 0xffff0000, v134
	v_lshlrev_b32_e32 v134, 16, v135
	v_lshlrev_b32_e32 v158, 16, v126
	v_pk_add_f32 v[172:173], v[172:173], v[172:173] op_sel_hi:[0,1]
	v_and_b32_e32 v135, 0xffff0000, v135
	v_and_b32_e32 v159, 0xffff0000, v126
	v_lshlrev_b32_e32 v126, 16, v127
	v_mul_f32_e32 v168, v154, v154
	v_mul_f32_e32 v170, v134, v134
	v_mul_f32_e32 v172, v158, v158
	v_and_b32_e32 v127, 0xffff0000, v127
	v_pk_fma_f32 v[168:169], v[154:155], v[154:155], v[168:169] op_sel_hi:[1,1,0]
	v_pk_fma_f32 v[170:171], v[134:135], v[134:135], v[170:171] op_sel_hi:[1,1,0]
	v_pk_fma_f32 v[174:175], v[158:159], v[158:159], v[172:173] op_sel_hi:[1,1,0]
	v_mul_f32_e32 v172, v126, v126
	v_lshlrev_b32_e32 v160, 16, v128
	v_and_b32_e32 v161, 0xffff0000, v128
	v_lshlrev_b32_e32 v128, 16, v129
	v_and_b32_e32 v129, 0xffff0000, v129
	v_pk_fma_f32 v[176:177], v[126:127], v[126:127], v[172:173] op_sel_hi:[1,1,0]
	v_pk_add_f32 v[168:169], v[168:169], v[170:171]
	v_mul_f32_e32 v172, v161, v161
	v_mul_f32_e32 v174, v128, v128
	v_mul_f32_e32 v176, v129, v129
	v_mul_f32_e32 v178, v160, v160
	v_mov_b32_e32 v179, v169
	v_pk_add_f32 v[168:169], v[178:179], v[172:173]
	v_pk_add_f32 v[170:171], v[174:175], v[176:177]
	v_lshlrev_b32_e32 v162, 16, v130
	v_pk_add_f32 v[168:169], v[168:169], v[170:171]
	v_and_b32_e32 v163, 0xffff0000, v130
	v_add_f32_e32 v168, v168, v169
	v_lshlrev_b32_e32 v130, 16, v131
	v_and_b32_e32 v131, 0xffff0000, v131
	v_add_f32_dpp v168, v168, v168 quad_perm:[1,0,3,2] row_mask:0xf bank_mask:0xf bound_ctrl:1
	v_lshlrev_b32_e32 v165, 16, v133
	v_lshlrev_b32_e32 v164, 16, v132
	v_add_f32_dpp v168, v168, v168 quad_perm:[2,3,0,1] row_mask:0xf bank_mask:0xf bound_ctrl:1
	v_and_b32_e32 v133, 0xffff0000, v133
	v_and_b32_e32 v132, 0xffff0000, v132
	v_add_f32_dpp v168, v168, v168 row_half_mirror row_mask:0xf bank_mask:0xf bound_ctrl:1
	v_lshlrev_b32_e32 v166, 16, v122
	v_and_b32_e32 v167, 0xffff0000, v122
	v_add_f32_dpp v170, v168, v168 row_mirror row_mask:0xf bank_mask:0xf bound_ctrl:1
	v_mbcnt_lo_u32_b32 v168, -1, 0
	v_mbcnt_hi_u32_b32 v168, -1, v168
	v_lshlrev_b32_e32 v122, 16, v123
	v_lshlrev_b32_e32 v168, 2, v168
	v_xor_b32_e32 v168, 64, v168
	ds_bpermute_b32 v171, v168, v170
	v_pk_mul_f32 v[178:179], v[132:133], v[132:133]
	v_and_b32_e32 v123, 0xffff0000, v123
	v_pk_fma_f32 v[178:179], v[164:165], v[164:165], v[178:179]
	v_lshlrev_b32_e32 v168, 16, v124
	s_waitcnt lgkmcnt(0)
	v_add_f32_e32 v171, v170, v171
	v_mov_b32_e32 v173, v171
	v_mul_f32_e32 v170, v162, v162
	s_nop 1
	v_permlane32_swap_b32 v173, v171
	v_and_b32_e32 v169, 0xffff0000, v124
	v_pk_fma_f32 v[174:175], v[162:163], v[162:163], v[170:171] op_sel_hi:[1,1,0]
	v_mul_f32_e32 v170, v130, v130
	v_pk_fma_f32 v[176:177], v[130:131], v[130:131], v[170:171] op_sel_hi:[1,1,0]
	v_mul_f32_e32 v170, v166, v166
	v_pk_fma_f32 v[180:181], v[166:167], v[166:167], v[170:171] op_sel_hi:[1,1,0]
	v_mul_f32_e32 v170, v122, v122
	v_lshlrev_b32_e32 v124, 16, v125
	v_and_b32_e32 v125, 0xffff0000, v125
	v_pk_add_f32 v[178:179], v[178:179], v[178:179] op_sel_hi:[0,1]
	v_pk_fma_f32 v[182:183], v[122:123], v[122:123], v[170:171] op_sel_hi:[1,1,0]
	v_pk_add_f32 v[174:175], v[174:175], v[176:177]
	v_mul_f32_e32 v178, v169, v169
	v_mul_f32_e32 v180, v124, v124
	v_mul_f32_e32 v182, v125, v125
	v_mul_f32_e32 v184, v168, v168
	v_mov_b32_e32 v185, v175
	v_pk_add_f32 v[174:175], v[184:185], v[178:179]
	v_pk_add_f32 v[176:177], v[180:181], v[182:183]
	v_mbcnt_lo_u32_b32 v172, -1, 0
	v_mbcnt_hi_u32_b32 v172, -1, v172
	s_mov_b32 s12, 0x3a800000
	v_pk_add_f32 v[174:175], v[174:175], v[176:177]
	v_lshlrev_b32_e32 v172, 2, v172
	v_add_f32_e32 v170, v174, v175
	v_xor_b32_e32 v172, 64, v172
	s_ashr_i32 s17, s16, 31
	v_add_f32_dpp v170, v170, v170 quad_perm:[1,0,3,2] row_mask:0xf bank_mask:0xf bound_ctrl:1
	s_nop 1
	v_add_f32_dpp v170, v170, v170 quad_perm:[2,3,0,1] row_mask:0xf bank_mask:0xf bound_ctrl:1
	s_nop 1
	v_add_f32_dpp v170, v170, v170 row_half_mirror row_mask:0xf bank_mask:0xf bound_ctrl:1
	s_nop 1
	v_add_f32_dpp v170, v170, v170 row_mirror row_mask:0xf bank_mask:0xf bound_ctrl:1
	ds_bpermute_b32 v172, v172, v170
	s_waitcnt lgkmcnt(0)
	v_add_f32_e32 v172, v170, v172
	v_mov_b32_e32 v170, v172
	s_nop 1
	v_permlane32_swap_b32 v172, v170
	s_nop 0
	v_pk_add_f32 v[170:171], v[172:173], v[170:171]
	v_mov_b32_e32 v172, 0x358637bd
	v_pk_fma_f32 v[170:171], v[170:171], s[12:13], v[172:173] op_sel_hi:[1,0,0]
	s_nop 0
	v_mul_f32_e32 v172, 0x4b800000, v171
	v_cmp_gt_f32_e32 vcc, s59, v171
	v_cmp_gt_f32_e64 s[12:13], s59, v170
	s_nop 0
	v_cndmask_b32_e32 v171, v171, v172, vcc
	v_mul_f32_e32 v172, 0x4b800000, v170
	v_rsq_f32_e32 v171, v171
	v_cndmask_b32_e64 v170, v170, v172, s[12:13]
	v_rsq_f32_e32 v172, v170
	v_mul_f32_e32 v170, 0x45800000, v171
	v_cndmask_b32_e32 v170, v171, v170, vcc
	v_mul_f32_e32 v171, 0x45800000, v172
	v_cndmask_b32_e64 v172, v172, v171, s[12:13]
	v_pk_mul_f32 v[130:131], v[172:173], v[130:131] op_sel_hi:[0,1]
	v_pk_fma_f32 v[174:175], v[92:93], v[130:131], v[76:77]
	v_mov_b32_e32 v131, v136
	v_mov_b32_e32 v136, v157
	v_mov_b32_e32 v157, v132
	v_mov_b32_e32 v132, v165
	v_pk_mul_f32 v[132:133], v[172:173], v[132:133] op_sel_hi:[0,1]
	v_pk_mul_f32 v[126:127], v[170:171], v[126:127] op_sel_hi:[0,1]
	v_pk_mul_f32 v[122:123], v[172:173], v[122:123] op_sel_hi:[0,1]
	v_mov_b32_e32 v130, v156
	v_mov_b32_e32 v156, v164
	v_pk_fma_f32 v[164:165], v[96:97], v[132:133], v[80:81]
	v_pk_mul_f32 v[132:133], v[170:171], v[158:159] op_sel_hi:[0,1]
	v_pk_fma_f32 v[158:159], v[100:101], v[126:127], v[84:85]
	v_pk_mul_f32 v[126:127], v[172:173], v[166:167] op_sel_hi:[0,1]
	v_pk_fma_f32 v[166:167], v[100:101], v[122:123], v[84:85]
	v_pk_mul_f32 v[122:123], v[170:171], v[160:161] op_sel_hi:[0,1]
	v_pk_mul_f32 v[154:155], v[170:171], v[154:155] op_sel_hi:[0,1]
	v_pk_mul_f32 v[134:135], v[170:171], v[134:135] op_sel_hi:[0,1]
	v_pk_mul_f32 v[130:131], v[170:171], v[130:131] op_sel_hi:[0,1]
	v_pk_mul_f32 v[136:137], v[170:171], v[136:137] op_sel_hi:[0,1]
	v_pk_fma_f32 v[176:177], v[98:99], v[126:127], v[82:83]
	v_pk_mul_f32 v[126:127], v[170:171], v[128:129] op_sel_hi:[0,1]
	v_pk_fma_f32 v[170:171], v[102:103], v[122:123], v[86:87]
	v_pk_mul_f32 v[122:123], v[172:173], v[168:169] op_sel_hi:[0,1]
	v_pk_mul_f32 v[124:125], v[172:173], v[124:125] op_sel_hi:[0,1]
	v_pk_fma_f32 v[154:155], v[90:91], v[154:155], v[74:75]
	v_pk_mul_f32 v[162:163], v[172:173], v[162:163] op_sel_hi:[0,1]
	v_pk_fma_f32 v[130:131], v[94:95], v[130:131], v[78:79]
	v_pk_mul_f32 v[156:157], v[172:173], v[156:157] op_sel_hi:[0,1]
	v_pk_fma_f32 v[132:133], v[98:99], v[132:133], v[82:83]
	v_pk_fma_f32 v[168:169], v[104:105], v[124:125], v[88:89]
	v_pk_fma_f32 v[172:173], v[102:103], v[122:123], v[86:87]
	v_mov_b32_e32 v122, v1
	v_mov_b32_e32 v123, v1
	v_mov_b32_e32 v124, v1
	v_mov_b32_e32 v125, v1
	v_cvt_pk_fp8_f32 v122, v154, v155
	v_cvt_pk_fp8_f32 v123, v130, v131
	v_cvt_pk_fp8_f32 v124, v132, v133
	v_cvt_pk_fp8_f32 v125, v170, v171
	v_pk_fma_f32 v[134:135], v[92:93], v[134:135], v[76:77]
	v_pk_fma_f32 v[136:137], v[96:97], v[136:137], v[80:81]
	v_pk_fma_f32 v[160:161], v[104:105], v[126:127], v[88:89]
	v_cvt_pk_fp8_f32 v122, v134, v135 op_sel:[0,0,1]
	v_cvt_pk_fp8_f32 v123, v136, v137 op_sel:[0,0,1]
	v_cvt_pk_fp8_f32 v124, v158, v159 op_sel:[0,0,1]
	v_cvt_pk_fp8_f32 v125, v160, v161 op_sel:[0,0,1]
	s_lshl_b64 s[12:13], s[16:17], 10
	v_lshl_add_u64 v[126:127], v[142:143], 0, s[12:13]
	v_pk_fma_f32 v[162:163], v[90:91], v[162:163], v[74:75]
	global_store_dwordx4 v[126:127], v[122:125], off
	v_pk_fma_f32 v[156:157], v[94:95], v[156:157], v[78:79]
	s_or_b32 s12, s16, 1
	v_cvt_pk_bf16_f32 v122, v154, v155
	v_lshlrev_b32_e32 v124, 16, v122
	v_and_b32_e32 v125, 0xffff0000, v122
	v_pk_add_f32 v[124:125], v[154:155], v[124:125] neg_lo:[0,1] neg_hi:[0,1]
	v_cvt_pk_bf16_f32 v123, v134, v135
	v_cvt_pk_bf16_f32 v126, v124, v125
	v_lshlrev_b32_e32 v124, 16, v123
	v_and_b32_e32 v125, 0xffff0000, v123
	v_pk_add_f32 v[124:125], v[134:135], v[124:125] neg_lo:[0,1] neg_hi:[0,1]
	s_ashr_i32 s13, s12, 31
	v_cvt_pk_bf16_f32 v127, v124, v125
	v_cvt_pk_bf16_f32 v124, v130, v131
	v_lshlrev_b32_e32 v128, 16, v124
	v_and_b32_e32 v129, 0xffff0000, v124
	v_cvt_pk_bf16_f32 v125, v136, v137
	v_pk_add_f32 v[128:129], v[130:131], v[128:129] neg_lo:[0,1] neg_hi:[0,1]
	v_lshlrev_b32_e32 v130, 16, v125
	v_and_b32_e32 v131, 0xffff0000, v125
	v_pk_add_f32 v[130:131], v[136:137], v[130:131] neg_lo:[0,1] neg_hi:[0,1]
	v_cvt_pk_bf16_f32 v128, v128, v129
	v_cvt_pk_bf16_f32 v129, v130, v131
	v_cvt_pk_bf16_f32 v130, v132, v133
	v_lshlrev_b32_e32 v134, 16, v130
	v_and_b32_e32 v135, 0xffff0000, v130
	v_pk_add_f32 v[132:133], v[132:133], v[134:135] neg_lo:[0,1] neg_hi:[0,1]
	v_cvt_pk_bf16_f32 v131, v158, v159
	v_cvt_pk_bf16_f32 v134, v132, v133
	v_lshlrev_b32_e32 v132, 16, v131
	v_and_b32_e32 v133, 0xffff0000, v131
	v_pk_add_f32 v[132:133], v[158:159], v[132:133] neg_lo:[0,1] neg_hi:[0,1]
	s_lshl_b64 s[12:13], s[12:13], 10
	v_cvt_pk_bf16_f32 v135, v132, v133
	v_cvt_pk_bf16_f32 v132, v170, v171
	v_cvt_pk_bf16_f32 v133, v160, v161
	v_lshlrev_b32_e32 v136, 16, v132
	v_and_b32_e32 v137, 0xffff0000, v132
	v_lshlrev_b32_e32 v154, 16, v133
	v_and_b32_e32 v155, 0xffff0000, v133
	v_pk_add_f32 v[136:137], v[170:171], v[136:137] neg_lo:[0,1] neg_hi:[0,1]
	v_pk_add_f32 v[154:155], v[160:161], v[154:155] neg_lo:[0,1] neg_hi:[0,1]
	v_cvt_pk_bf16_f32 v136, v136, v137
	v_cvt_pk_bf16_f32 v137, v154, v155
	v_add_u32_e32 v154, s23, v149
	ds_write_b128 v154, v[122:125]
	ds_write_b128 v154, v[130:133] offset:16
	ds_write_b128 v154, v[126:129] offset:33024
	ds_write_b128 v154, v[134:137] offset:33040
	v_mov_b32_e32 v122, v1
	v_mov_b32_e32 v123, v1
	v_mov_b32_e32 v124, v1
	v_mov_b32_e32 v125, v1
	v_cvt_pk_fp8_f32 v122, v162, v163
	v_cvt_pk_fp8_f32 v123, v156, v157
	v_cvt_pk_fp8_f32 v124, v176, v177
	v_cvt_pk_fp8_f32 v125, v172, v173
	v_cvt_pk_fp8_f32 v122, v174, v175 op_sel:[0,0,1]
	v_cvt_pk_fp8_f32 v123, v164, v165 op_sel:[0,0,1]
	v_cvt_pk_fp8_f32 v124, v166, v167 op_sel:[0,0,1]
	v_cvt_pk_fp8_f32 v125, v168, v169 op_sel:[0,0,1]
	v_lshl_add_u64 v[126:127], v[142:143], 0, s[12:13]
	v_cmp_lt_i32_e32 vcc, -1, v153
	global_store_dwordx4 v[126:127], v[122:125], off
	s_nop 1
	v_cvt_pk_bf16_f32 v122, v162, v163
	v_lshlrev_b32_e32 v124, 16, v122
	v_and_b32_e32 v125, 0xffff0000, v122
	v_pk_add_f32 v[124:125], v[162:163], v[124:125] neg_lo:[0,1] neg_hi:[0,1]
	v_cvt_pk_bf16_f32 v123, v174, v175
	v_cvt_pk_bf16_f32 v126, v124, v125
	v_lshlrev_b32_e32 v124, 16, v123
	v_and_b32_e32 v125, 0xffff0000, v123
	v_pk_add_f32 v[124:125], v[174:175], v[124:125] neg_lo:[0,1] neg_hi:[0,1]
	s_nop 0
	v_cvt_pk_bf16_f32 v127, v124, v125
	v_cvt_pk_bf16_f32 v124, v156, v157
	v_cvt_pk_bf16_f32 v125, v164, v165
	v_lshlrev_b32_e32 v128, 16, v124
	v_and_b32_e32 v129, 0xffff0000, v124
	v_lshlrev_b32_e32 v130, 16, v125
	v_and_b32_e32 v131, 0xffff0000, v125
	v_pk_add_f32 v[128:129], v[156:157], v[128:129] neg_lo:[0,1] neg_hi:[0,1]
	v_pk_add_f32 v[130:131], v[164:165], v[130:131] neg_lo:[0,1] neg_hi:[0,1]
	v_cvt_pk_bf16_f32 v128, v128, v129
	v_cvt_pk_bf16_f32 v129, v130, v131
	v_cvt_pk_bf16_f32 v130, v176, v177
	v_lshlrev_b32_e32 v132, 16, v130
	v_and_b32_e32 v133, 0xffff0000, v130
	v_pk_add_f32 v[132:133], v[176:177], v[132:133] neg_lo:[0,1] neg_hi:[0,1]
	v_cvt_pk_bf16_f32 v131, v166, v167
	v_cvt_pk_bf16_f32 v134, v132, v133
	v_lshlrev_b32_e32 v132, 16, v131
	v_and_b32_e32 v133, 0xffff0000, v131
	v_pk_add_f32 v[132:133], v[166:167], v[132:133] neg_lo:[0,1] neg_hi:[0,1]
	s_nop 0
	v_cvt_pk_bf16_f32 v135, v132, v133
	v_cvt_pk_bf16_f32 v132, v172, v173
	v_cvt_pk_bf16_f32 v133, v168, v169
	v_lshlrev_b32_e32 v136, 16, v132
	v_and_b32_e32 v137, 0xffff0000, v132
	v_lshlrev_b32_e32 v154, 16, v133
	v_and_b32_e32 v155, 0xffff0000, v133
	v_pk_add_f32 v[136:137], v[172:173], v[136:137] neg_lo:[0,1] neg_hi:[0,1]
	v_pk_add_f32 v[154:155], v[168:169], v[154:155] neg_lo:[0,1] neg_hi:[0,1]
	v_cvt_pk_bf16_f32 v136, v136, v137
	v_cvt_pk_bf16_f32 v137, v154, v155
	v_add_u32_e32 v154, s24, v149
	ds_write_b128 v154, v[122:125]
	ds_write_b128 v154, v[130:133] offset:16
	ds_write_b128 v154, v[126:129] offset:33024
	ds_write_b128 v154, v[134:137] offset:33040
	s_and_saveexec_b64 s[12:13], vcc
	s_cbranch_execz .LBB0_1549
	s_mov_b32 s14, 35
	s_ashr_i32 s15, s14, 31
	s_lshl_b64 s[14:15], s[14:15], 3
	s_add_u32 s14, s0, s14
	s_addc_u32 s15, s1, s15
	s_load_dwordx2 s[14:15], s[14:15], 0x0
	v_lshlrev_b32_e32 v122, 2, v153
	v_mov_b32_e32 v123, v1
	v_lshlrev_b64 v[122:123], 2, v[122:123]
	v_mov_b32_e32 v153, -1
	s_waitcnt lgkmcnt(0)
	v_lshl_add_u64 v[124:125], s[14:15], 0, v[122:123]
	v_add_co_u32_e32 v124, vcc, s85, v124
	s_mov_b32 s14, 35
	s_nop 0
	v_addc_co_u32_e32 v125, vcc, 0, v125, vcc
	global_store_dwordx4 v[124:125], v[70:73], off
	s_ashr_i32 s15, s14, 31
	s_lshl_b64 s[14:15], s[14:15], 3
	s_add_u32 s14, s0, s14
	s_addc_u32 s15, s1, s15
	s_load_dwordx2 s[14:15], s[14:15], 0x0
	s_waitcnt lgkmcnt(0)
	v_lshl_add_u64 v[122:123], s[14:15], 0, v[122:123]
	v_add_co_u32_e32 v122, vcc, 0xa00000, v122
	s_nop 1
	v_addc_co_u32_e32 v123, vcc, 0, v123, vcc
	global_store_dwordx4 v[122:123], v[66:69], off
.LBB0_1549:
	s_or_b64 exec, exec, s[12:13]
	s_waitcnt lgkmcnt(0)
	s_barrier
	ds_read_b128 v[122:125], v151
	ds_read_b128 v[126:129], v151 offset:33024
	s_waitcnt lgkmcnt(1)
	v_mfma_f32_16x16x32_bf16 v[130:133], v[122:125], v[2:5], 0
	v_mfma_f32_16x16x32_bf16 v[134:137], v[122:125], v[10:13], 0
	v_mfma_f32_16x16x32_bf16 v[130:133], v[122:125], v[6:9], v[130:133]
	v_mfma_f32_16x16x32_bf16 v[122:125], v[122:125], v[14:17], v[134:137]
	s_waitcnt lgkmcnt(0)
	v_mfma_f32_16x16x32_bf16 v[130:133], v[126:129], v[2:5], v[130:133]
	v_mfma_f32_16x16x32_bf16 v[122:125], v[126:129], v[10:13], v[122:125]
	ds_read_b128 v[126:129], v151 offset:64
	s_nop 1
	ds_read_b128 v[134:137], v151 offset:33088
	s_waitcnt lgkmcnt(1)
	v_mfma_f32_16x16x32_bf16 v[130:133], v[126:129], v[18:21], v[130:133]
	v_mfma_f32_16x16x32_bf16 v[122:125], v[126:129], v[26:29], v[122:125]
	v_mfma_f32_16x16x32_bf16 v[130:133], v[126:129], v[22:25], v[130:133]
	v_mfma_f32_16x16x32_bf16 v[122:125], v[126:129], v[30:33], v[122:125]
	s_waitcnt lgkmcnt(0)
	v_mfma_f32_16x16x32_bf16 v[130:133], v[134:137], v[18:21], v[130:133]
	v_mfma_f32_16x16x32_bf16 v[122:125], v[134:137], v[26:29], v[122:125]
	ds_read_b128 v[126:129], v151 offset:128
	ds_read_b128 v[134:137], v151 offset:33152
	s_waitcnt lgkmcnt(1)
	v_mfma_f32_16x16x32_bf16 v[130:133], v[126:129], v[34:37], v[130:133]
	v_mfma_f32_16x16x32_bf16 v[122:125], v[126:129], v[42:45], v[122:125]
	v_mfma_f32_16x16x32_bf16 v[130:133], v[126:129], v[38:41], v[130:133]
	v_mfma_f32_16x16x32_bf16 v[122:125], v[126:129], v[46:49], v[122:125]
	s_waitcnt lgkmcnt(0)
	v_mfma_f32_16x16x32_bf16 v[130:133], v[134:137], v[34:37], v[130:133]
	v_mfma_f32_16x16x32_bf16 v[122:125], v[134:137], v[42:45], v[122:125]
	ds_read_b128 v[126:129], v151 offset:192
	ds_read_b128 v[134:137], v151 offset:33216
	s_waitcnt lgkmcnt(1)
	v_mfma_f32_16x16x32_bf16 v[130:133], v[126:129], v[50:53], v[130:133]
	v_mfma_f32_16x16x32_bf16 v[122:125], v[126:129], v[58:61], v[122:125]
	v_mfma_f32_16x16x32_bf16 v[130:133], v[126:129], v[54:57], v[130:133]
	v_mfma_f32_16x16x32_bf16 v[122:125], v[126:129], v[62:65], v[122:125]
	v_mov_b32_e32 v126, v1
	v_mov_b32_e32 v127, v1
	v_add_u32_e32 v128, s25, v150
	s_waitcnt lgkmcnt(0)
	v_mfma_f32_16x16x32_bf16 v[130:133], v[134:137], v[50:53], v[130:133]
	v_mfma_f32_16x16x32_bf16 v[122:125], v[134:137], v[58:61], v[122:125]
	s_nop 7
	ds_write2_b32 v152, v130, v122 offset1:16
	ds_write2_b32 v152, v131, v123 offset0:32 offset1:48
	ds_write2_b32 v152, v132, v124 offset0:64 offset1:80
	ds_write2_b32 v152, v133, v125 offset0:96 offset1:112
	v_add_u32_e32 v124, s22, v150
	s_waitcnt lgkmcnt(0)
	s_barrier
	ds_read2st64_b32 v[122:123], v124 offset1:8
	ds_read2st64_b32 v[126:127], v124 offset0:16 offset1:24
	ds_read2st64_b32 v[128:129], v124 offset0:32 offset1:40
	ds_read2st64_b32 v[130:131], v124 offset0:48 offset1:56
	s_waitcnt lgkmcnt(3)
	v_add_f32_e32 v122, v148, v122
	v_add_f32_e32 v122, v122, v123
	s_waitcnt lgkmcnt(2)
	v_add_f32_e32 v122, v122, v126
	v_add_f32_e32 v122, v122, v127
	s_waitcnt lgkmcnt(1)
	v_add_f32_e32 v122, v122, v128
	v_add_f32_e32 v122, v122, v129
	s_waitcnt lgkmcnt(0)
	v_add_f32_e32 v122, v122, v130
	v_add_f32_e32 v122, v122, v131
	s_nop 1
	v_max_f32_dpp v123, v122, v122 quad_perm:[1,0,3,2] row_mask:0xf bank_mask:0xf
	s_nop 1
	v_max_f32_dpp v123, v123, v123 quad_perm:[2,3,0,1] row_mask:0xf bank_mask:0xf
	s_nop 1
	v_max_f32_dpp v123, v123, v123 row_half_mirror row_mask:0xf bank_mask:0xf
	s_nop 1
	v_max_f32_dpp v123, v123, v123 row_mirror row_mask:0xf bank_mask:0xf
	v_mov_b32_e32 v125, v123
	s_nop 1
	v_permlane16_swap_b32 v123, v125
	s_nop 1
	v_max_f32_e32 v126, v123, v125
	v_cmp_eq_f32_e32 vcc, v122, v126
	s_nop 0
	s_ff1_i32_b32 s17, vcc_lo
	s_ff1_i32_b32 s31, vcc_hi
	s_lshl_b32 s36, 1, s17
	s_lshl_b32 s37, 1, s31
	s_nop 0
	v_cndmask_b32_e64 v122, v122, v220, s[36:37]
	s_nop 1
	v_max_f32_dpp v123, v122, v122 quad_perm:[1,0,3,2] row_mask:0xf bank_mask:0xf
	s_nop 1
	v_max_f32_dpp v123, v123, v123 quad_perm:[2,3,0,1] row_mask:0xf bank_mask:0xf
	s_nop 1
	v_max_f32_dpp v123, v123, v123 row_half_mirror row_mask:0xf bank_mask:0xf
	s_nop 1
	v_max_f32_dpp v123, v123, v123 row_mirror row_mask:0xf bank_mask:0xf
	v_mov_b32_e32 v125, v123
	s_nop 1
	v_permlane16_swap_b32 v123, v125
	s_nop 1
	v_max_f32_e32 v127, v123, v125
	v_cmp_eq_f32_e32 vcc, v122, v127
	s_nop 0
	s_ff1_i32_b32 s29, vcc_lo
	s_ff1_i32_b32 s34, vcc_hi
	s_lshl_b32 s36, 1, s29
	s_lshl_b32 s37, 1, s34
	s_nop 0
	v_cndmask_b32_e64 v122, v122, v220, s[36:37]
	s_nop 1
	v_max_f32_dpp v123, v122, v122 quad_perm:[1,0,3,2] row_mask:0xf bank_mask:0xf
	s_nop 1
	v_max_f32_dpp v123, v123, v123 quad_perm:[2,3,0,1] row_mask:0xf bank_mask:0xf
	s_nop 1
	v_max_f32_dpp v123, v123, v123 row_half_mirror row_mask:0xf bank_mask:0xf
	s_nop 1
	v_max_f32_dpp v123, v123, v123 row_mirror row_mask:0xf bank_mask:0xf
	v_mov_b32_e32 v125, v123
	s_nop 1
	v_permlane16_swap_b32 v123, v125
	s_nop 1
	v_max_f32_e32 v128, v123, v125
	v_cmp_eq_f32_e32 vcc, v122, v128
	s_nop 0
	s_ff1_i32_b32 s30, vcc_lo
	s_ff1_i32_b32 s35, vcc_hi
	s_lshl_b32 s36, 1, s30
	s_lshl_b32 s37, 1, s35
	s_nop 0
	v_cndmask_b32_e64 v122, v122, v220, s[36:37]
	s_nop 1
	v_max_f32_dpp v123, v122, v122 quad_perm:[1,0,3,2] row_mask:0xf bank_mask:0xf
	s_nop 1
	v_max_f32_dpp v123, v123, v123 quad_perm:[2,3,0,1] row_mask:0xf bank_mask:0xf
	s_nop 1
	v_max_f32_dpp v123, v123, v123 row_half_mirror row_mask:0xf bank_mask:0xf
	s_nop 1
	v_max_f32_dpp v123, v123, v123 row_mirror row_mask:0xf bank_mask:0xf
	v_mov_b32_e32 v125, v123
	s_nop 1
	v_permlane16_swap_b32 v123, v125
	s_nop 1
	v_max_f32_e32 v129, v123, v125
	v_cmp_eq_f32_e32 vcc, v122, v129
	s_nop 0
	s_ff1_i32_b32 s12, vcc_lo
	s_ff1_i32_b32 s14, vcc_hi
	v_sub_f32_e32 v130, v127, v126
	v_sub_f32_e32 v131, v128, v126
	v_sub_f32_e32 v132, v129, v126
	v_mul_f32_e32 v130, 0x3fb8aa3b, v130
	v_mul_f32_e32 v131, 0x3fb8aa3b, v131
	v_mul_f32_e32 v132, 0x3fb8aa3b, v132
	v_exp_f32_e32 v67, v130
	v_exp_f32_e32 v68, v131
	v_exp_f32_e32 v69, v132
	v_lshrrev_b32_e32 v125, 5, v147
	v_writelane_b32 v70, s17, 0
	v_writelane_b32 v70, s31, 32
	v_add_f32_e32 v133, 1.0, v67
	v_add_f32_e32 v133, v133, v68
	v_add_f32_e32 v133, v133, v69
	v_div_scale_f32 v134, s[18:19], v133, v133, 1.0
	v_rcp_f32_e32 v135, v134
	v_writelane_b32 v71, s29, 0
	v_writelane_b32 v71, s34, 32
	v_fma_f32 v136, -v134, v135, 1.0
	v_fmac_f32_e32 v135, v136, v135
	v_div_scale_f32 v136, vcc, 1.0, v133, 1.0
	v_mul_f32_e32 v137, v136, v135
	v_fma_f32 v130, -v134, v137, v136
	v_fmac_f32_e32 v137, v130, v135
	v_fma_f32 v134, -v134, v137, v136
	v_div_fmas_f32 v134, v134, v135, v137
	v_writelane_b32 v72, s30, 0
	v_writelane_b32 v72, s35, 32
	v_writelane_b32 v73, s12, 0
	v_writelane_b32 v73, s14, 32
	v_div_fixup_f32 v66, v134, v133, 1.0
	v_mul_f32_e32 v67, v67, v66
	v_mul_f32_e32 v68, v68, v66
	v_mul_f32_e32 v69, v69, v66
	s_mov_b32 exec_lo, 1
	s_mov_b32 exec_hi, 1
	s_mov_b32 s13, 0x20000
	v_or_b32_e32 v153, s16, v125
	v_lshl_add_u32 v130, v70, 2, s13
	v_lshl_add_u32 v131, v71, 2, s13
	v_lshl_add_u32 v132, v72, 2, s13
	v_lshl_add_u32 v133, v73, 2, s13
	ds_add_u32 v130, v205
	ds_add_u32 v131, v205
	ds_add_u32 v132, v205
	ds_add_u32 v133, v205
	s_mov_b64 exec, -1
	s_add_i32 s26, s26, 16
	s_cmp_eq_u32 s21, s27
	s_cbranch_scc1 .LBB0_1554
	s_waitcnt vmcnt(0)
	v_mov_b64_e32 v[136:137], v[112:113]
	v_mov_b64_e32 v[128:129], v[108:109]
	v_mov_b64_e32 v[132:133], v[120:121]
	v_mov_b64_e32 v[124:125], v[116:117]
	v_mov_b64_e32 v[134:135], v[110:111]
	v_mov_b64_e32 v[126:127], v[106:107]
	v_mov_b64_e32 v[130:131], v[118:119]
	v_mov_b64_e32 v[122:123], v[114:115]
	s_branch .LBB0_1543
